# MoE phase prologues: row-table and bias-table gather loops de-serialised with a touch pass (all 9 gathers in flight before the loop that waits per gather); on top of v6
# speedup vs baseline: 1.0064x; 1.0011x over previous
.LBB0_1308:
	s_or_b64 exec, exec, s[0:1]
	s_movk_i32 s0, 0x1200
	v_mul_i32_i24_e32 v12, 0x400, v11
	v_cmp_gt_i32_e32 vcc, s0, v8
	v_and_b32_e32 v0, 0xff, v8
	s_waitcnt lgkmcnt(0)
	s_barrier
	s_and_saveexec_b64 s[0:1], vcc
	s_cbranch_execz .LBB0_1313
	s_add_u32 s10, s8, 0xc00000
	v_lshl_add_u32 v1, v8, 1, 0
	s_addc_u32 s11, s9, 0
	v_add_u32_e32 v1, 0x20600, v1
	s_mov_b64 s[12:13], 0
	s_movk_i32 s16, 0xfff
	v_mov_b32_e32 v2, v8
	s_mov_b64 s[66:67], exec
	s_branch .Lmt1_1311

.Lmt1_1311:
	v_ashrrev_i32_e32 v3, 6, v2
	v_lshlrev_b32_e32 v3, 2, v3
	v_and_b32_e32 v3, -16, v3
	v_add_u32_e32 v3, 0, v3
	v_add_u32_e32 v4, 0x20200, v3
	ds_read_b32 v3, v4
	s_waitcnt lgkmcnt(0)
	v_cmp_lt_i32_e64 s[4:5], -1, v3
	s_and_saveexec_b64 s[14:15], s[4:5]
	s_cbranch_execz .Lmt1_1310
	ds_read_b32 v4, v4 offset:8
	s_waitcnt lgkmcnt(0)
	v_lshl_add_u32 v5, v4, 2, 0
	v_add_u32_e32 v6, 0x20000, v5
	ds_read_b32 v6, v6
	v_add_u32_e32 v5, 0x20100, v5
	ds_read_b32 v5, v5
	s_waitcnt lgkmcnt(1)
	v_sub_u32_e32 v3, v3, v6
	v_lshl_or_b32 v3, v3, 8, v0
	s_waitcnt lgkmcnt(0)
	v_add_u32_e32 v5, -1, v5
	v_min_i32_e32 v3, v3, v5
	v_lshl_add_u32 v4, v4, 14, v3
	v_ashrrev_i32_e32 v5, 31, v4
	v_lshl_add_u64 v[4:5], v[4:5], 2, s[10:11]
	global_load_dword v250, v[4:5], off
	s_branch .Lmt1_1310
.Lmt1_done:
	s_mov_b64 exec, s[66:67]
	v_lshl_add_u32 v1, v8, 1, 0
	v_add_u32_e32 v1, 0x20600, v1
	s_mov_b64 s[12:13], 0
	v_mov_b32_e32 v2, v8
	s_branch .LBB0_1311

.LBB0_1313:
	s_or_b64 exec, exec, s[0:1]
	s_mov_b64 s[4:5], s[86:87]
	s_waitcnt lgkmcnt(0)
	s_barrier
	s_and_saveexec_b64 s[0:1], vcc
	s_cbranch_execz .LBB0_1322
	s_load_dwordx2 s[10:11], s[4:5], 0xf8
	s_load_dwordx2 s[12:13], s[4:5], 0x108
	s_movk_i32 s4, 0x7f
	v_lshl_add_u32 v1, v8, 2, 0
	s_movk_i32 s16, 0xfe00
	v_cmp_lt_u32_e32 vcc, s4, v0
	v_add_u32_e32 v13, 0x22a00, v1
	s_mov_b64 s[14:15], 0
	v_mov_b32_e32 v1, 0
	s_mov_b32 s17, -1
	s_movk_i32 s20, 0xfff
	v_lshlrev_b32_e32 v0, 2, v0
	v_mov_b32_e32 v14, v8
	s_mov_b64 s[66:67], exec
	s_branch .Lmt2_1317
.Lmt2_1315:
	s_or_b64 exec, exec, s[4:5]
	global_load_dword v250, v[4:5], off

.Lmt2_done:
	s_mov_b64 exec, s[66:67]
	v_lshl_add_u32 v13, v8, 2, 0
	v_add_u32_e32 v13, 0x22a00, v13
	s_mov_b64 s[14:15], 0
	v_mov_b32_e32 v14, v8
	s_branch .LBB0_1317

.LBB0_1404:
	s_or_b64 exec, exec, s[8:9]
	s_movk_i32 s4, 0x1200
	v_mul_i32_i24_e32 v2, 0x400, v9
	v_cmp_gt_i32_e32 vcc, s4, v8
	s_mov_b64 s[8:9], s[86:87]
	s_waitcnt lgkmcnt(0)
	s_barrier
	s_and_saveexec_b64 s[4:5], vcc
	s_cbranch_execz .LBB0_1409
	s_load_dwordx2 s[8:9], s[8:9], 0x118
	v_and_b32_e32 v0, 0xff, v8
	v_lshl_add_u32 v3, v8, 2, 0
	v_mov_b32_e32 v1, 0
	v_add_u32_e32 v3, 0x22a00, v3
	s_mov_b64 s[10:11], 0
	v_lshlrev_b32_e32 v0, 2, v0
	s_movk_i32 s14, 0xfff
	v_mov_b32_e32 v6, v8
	s_mov_b64 s[66:67], exec
	s_branch .Lmt3_1407

.Lmt3_1407:
	v_ashrrev_i32_e32 v7, 6, v6
	v_lshlrev_b32_e32 v7, 2, v7
	v_and_b32_e32 v7, -16, v7
	v_add_u32_e32 v7, 0, v7
	v_add_u32_e32 v7, 0x20200, v7
	ds_read_b32 v10, v7
	s_waitcnt lgkmcnt(0)
	v_cmp_lt_i32_e32 vcc, -1, v10
	s_and_saveexec_b64 s[12:13], vcc
	s_cbranch_execz .Lmt3_1406
	ds_read2_b32 v[10:11], v7 offset0:1 offset1:2
	s_waitcnt lgkmcnt(0)
	v_ashrrev_i32_e32 v13, 31, v11
	v_mov_b32_e32 v12, v11
	v_lshlrev_b32_e32 v10, 8, v10
	v_lshlrev_b64 v[12:13], 13, v[12:13]
	v_ashrrev_i32_e32 v11, 31, v10
	v_lshl_add_u64 v[12:13], s[8:9], 0, v[12:13]
	v_lshl_add_u64 v[10:11], v[10:11], 2, v[12:13]
	v_lshl_add_u64 v[10:11], v[10:11], 0, v[0:1]
	global_load_dword v250, v[10:11], off
	s_branch .Lmt3_1406
.Lmt3_done:
	s_mov_b64 exec, s[66:67]
	v_lshl_add_u32 v3, v8, 2, 0
	v_add_u32_e32 v3, 0x22a00, v3
	s_mov_b64 s[10:11], 0
	v_mov_b32_e32 v6, v8
	s_branch .LBB0_1407
